# v12 + P3 S5 chunk scan: all 4x16 chunk-state loads of both scan passes issued up front (global instead of flat, counted waits) instead of a full drain per 8-chunk step
# baseline (speedup 1.0000x reference)
.LBB0_510:
	v_mov_b32_e32 v54, 0x4f200000
	v_mov_b32_e32 v55, 0
	v_lshl_add_u64 v[52:53], v[16:17], 0, v[54:55]
	global_load_dword v132, v[52:53], off
	global_load_dword v133, v[52:53], off offset:256
	global_load_dword v134, v[52:53], off offset:512
	global_load_dword v135, v[52:53], off offset:768
	global_load_dword v136, v[52:53], off offset:1024
	global_load_dword v137, v[52:53], off offset:1280
	global_load_dword v138, v[52:53], off offset:1536
	global_load_dword v139, v[52:53], off offset:1792
	global_load_dword v140, v[52:53], off offset:2048
	global_load_dword v141, v[52:53], off offset:2304
	global_load_dword v142, v[52:53], off offset:2560
	global_load_dword v143, v[52:53], off offset:2816
	global_load_dword v144, v[52:53], off offset:3072
	global_load_dword v145, v[52:53], off offset:3328
	global_load_dword v146, v[52:53], off offset:3584
	global_load_dword v147, v[52:53], off offset:3840
	v_lshl_add_u64 v[52:53], v[52:53], 0, s[4:5]
	global_load_dword v148, v[52:53], off
	global_load_dword v149, v[52:53], off offset:256
	global_load_dword v150, v[52:53], off offset:512
	global_load_dword v151, v[52:53], off offset:768
	global_load_dword v152, v[52:53], off offset:1024
	global_load_dword v153, v[52:53], off offset:1280
	global_load_dword v154, v[52:53], off offset:1536
	global_load_dword v155, v[52:53], off offset:1792
	global_load_dword v156, v[52:53], off offset:2048
	global_load_dword v157, v[52:53], off offset:2304
	global_load_dword v158, v[52:53], off offset:2560
	global_load_dword v159, v[52:53], off offset:2816
	global_load_dword v160, v[52:53], off offset:3072
	global_load_dword v161, v[52:53], off offset:3328
	global_load_dword v162, v[52:53], off offset:3584
	global_load_dword v163, v[52:53], off offset:3840
	v_lshl_add_u64 v[52:53], v[52:53], 0, s[4:5]
	global_load_dword v164, v[52:53], off
	global_load_dword v165, v[52:53], off offset:256
	global_load_dword v166, v[52:53], off offset:512
	global_load_dword v167, v[52:53], off offset:768
	global_load_dword v168, v[52:53], off offset:1024
	global_load_dword v169, v[52:53], off offset:1280
	global_load_dword v170, v[52:53], off offset:1536
	global_load_dword v171, v[52:53], off offset:1792
	global_load_dword v172, v[52:53], off offset:2048
	global_load_dword v173, v[52:53], off offset:2304
	global_load_dword v174, v[52:53], off offset:2560
	global_load_dword v175, v[52:53], off offset:2816
	global_load_dword v176, v[52:53], off offset:3072
	global_load_dword v177, v[52:53], off offset:3328
	global_load_dword v178, v[52:53], off offset:3584
	global_load_dword v179, v[52:53], off offset:3840
	v_lshl_add_u64 v[52:53], v[52:53], 0, s[4:5]
	global_load_dword v200, v[52:53], off
	global_load_dword v201, v[52:53], off offset:256
	global_load_dword v202, v[52:53], off offset:512
	global_load_dword v203, v[52:53], off offset:768
	global_load_dword v204, v[52:53], off offset:1024
	global_load_dword v205, v[52:53], off offset:1280
	global_load_dword v206, v[52:53], off offset:1536
	global_load_dword v207, v[52:53], off offset:1792
	global_load_dword v208, v[52:53], off offset:2048
	global_load_dword v209, v[52:53], off offset:2304
	global_load_dword v210, v[52:53], off offset:2560
	global_load_dword v211, v[52:53], off offset:2816
	global_load_dword v212, v[52:53], off offset:3072
	global_load_dword v213, v[52:53], off offset:3328
	global_load_dword v214, v[52:53], off offset:3584
	global_load_dword v215, v[52:53], off offset:3840
	v_pk_mul_f32 v[20:21], v[12:13], v[18:19] op_sel:[0,1]
	v_pk_fma_f32 v[44:45], v[10:11], v[18:19], v[20:21] neg_lo:[0,0,1] neg_hi:[0,0,1]
	v_pk_fma_f32 v[18:19], v[10:11], v[18:19], v[20:21] op_sel_hi:[1,0,1]
	v_mov_b32_e32 v45, v19
	s_waitcnt vmcnt(48) lgkmcnt(0)
	v_pk_add_f32 v[18:19], v[44:45], v[132:133]
	s_nop 0
	v_pk_mul_f32 v[20:21], v[12:13], v[18:19] op_sel:[0,1]
	s_nop 0
	v_pk_fma_f32 v[28:29], v[10:11], v[18:19], v[20:21] neg_lo:[0,0,1] neg_hi:[0,0,1]
	v_pk_fma_f32 v[18:19], v[10:11], v[18:19], v[20:21] op_sel_hi:[1,0,1]
	s_nop 0
	v_mov_b32_e32 v29, v19
	v_pk_add_f32 v[18:19], v[28:29], v[134:135]
	s_nop 0
	v_pk_mul_f32 v[20:21], v[12:13], v[18:19] op_sel:[0,1]
	s_nop 0
	v_pk_fma_f32 v[28:29], v[10:11], v[18:19], v[20:21] neg_lo:[0,0,1] neg_hi:[0,0,1]
	v_pk_fma_f32 v[18:19], v[10:11], v[18:19], v[20:21] op_sel_hi:[1,0,1]
	s_nop 0
	v_mov_b32_e32 v29, v19
	v_pk_add_f32 v[18:19], v[28:29], v[136:137]
	s_nop 0
	v_pk_mul_f32 v[20:21], v[12:13], v[18:19] op_sel:[0,1]
	s_nop 0
	v_pk_fma_f32 v[28:29], v[10:11], v[18:19], v[20:21] neg_lo:[0,0,1] neg_hi:[0,0,1]
	v_pk_fma_f32 v[18:19], v[10:11], v[18:19], v[20:21] op_sel_hi:[1,0,1]
	s_nop 0
	v_mov_b32_e32 v29, v19
	v_pk_add_f32 v[18:19], v[28:29], v[138:139]
	s_nop 0
	v_pk_mul_f32 v[20:21], v[12:13], v[18:19] op_sel:[0,1]
	s_nop 0
	v_pk_fma_f32 v[28:29], v[10:11], v[18:19], v[20:21] neg_lo:[0,0,1] neg_hi:[0,0,1]
	v_pk_fma_f32 v[18:19], v[10:11], v[18:19], v[20:21] op_sel_hi:[1,0,1]
	s_nop 0
	v_mov_b32_e32 v29, v19
	v_pk_add_f32 v[18:19], v[28:29], v[140:141]
	s_nop 0
	v_pk_mul_f32 v[20:21], v[12:13], v[18:19] op_sel:[0,1]
	s_nop 0
	v_pk_fma_f32 v[28:29], v[10:11], v[18:19], v[20:21] neg_lo:[0,0,1] neg_hi:[0,0,1]
	v_pk_fma_f32 v[18:19], v[10:11], v[18:19], v[20:21] op_sel_hi:[1,0,1]
	s_nop 0
	v_mov_b32_e32 v29, v19
	v_pk_add_f32 v[18:19], v[28:29], v[142:143]
	s_nop 0
	v_pk_mul_f32 v[20:21], v[12:13], v[18:19] op_sel:[0,1]
	s_nop 0
	v_pk_fma_f32 v[28:29], v[10:11], v[18:19], v[20:21] neg_lo:[0,0,1] neg_hi:[0,0,1]
	v_pk_fma_f32 v[18:19], v[10:11], v[18:19], v[20:21] op_sel_hi:[1,0,1]
	s_nop 0
	v_mov_b32_e32 v29, v19
	v_pk_add_f32 v[18:19], v[28:29], v[144:145]
	s_nop 0
	v_pk_mul_f32 v[20:21], v[12:13], v[18:19] op_sel:[0,1]
	s_nop 0
	v_pk_fma_f32 v[28:29], v[10:11], v[18:19], v[20:21] neg_lo:[0,0,1] neg_hi:[0,0,1]
	v_pk_fma_f32 v[18:19], v[10:11], v[18:19], v[20:21] op_sel_hi:[1,0,1]
	s_nop 0
	v_mov_b32_e32 v29, v19
	v_pk_add_f32 v[18:19], v[28:29], v[146:147]
	s_nop 0
	v_pk_mul_f32 v[20:21], v[12:13], v[18:19] op_sel:[0,1]
	v_pk_fma_f32 v[44:45], v[10:11], v[18:19], v[20:21] neg_lo:[0,0,1] neg_hi:[0,0,1]
	v_pk_fma_f32 v[18:19], v[10:11], v[18:19], v[20:21] op_sel_hi:[1,0,1]
	v_mov_b32_e32 v45, v19
	s_waitcnt vmcnt(32) lgkmcnt(0)
	v_pk_add_f32 v[18:19], v[44:45], v[148:149]
	s_nop 0
	v_pk_mul_f32 v[20:21], v[12:13], v[18:19] op_sel:[0,1]
	s_nop 0
	v_pk_fma_f32 v[28:29], v[10:11], v[18:19], v[20:21] neg_lo:[0,0,1] neg_hi:[0,0,1]
	v_pk_fma_f32 v[18:19], v[10:11], v[18:19], v[20:21] op_sel_hi:[1,0,1]
	s_nop 0
	v_mov_b32_e32 v29, v19
	v_pk_add_f32 v[18:19], v[28:29], v[150:151]
	s_nop 0
	v_pk_mul_f32 v[20:21], v[12:13], v[18:19] op_sel:[0,1]
	s_nop 0
	v_pk_fma_f32 v[28:29], v[10:11], v[18:19], v[20:21] neg_lo:[0,0,1] neg_hi:[0,0,1]
	v_pk_fma_f32 v[18:19], v[10:11], v[18:19], v[20:21] op_sel_hi:[1,0,1]
	s_nop 0
	v_mov_b32_e32 v29, v19
	v_pk_add_f32 v[18:19], v[28:29], v[152:153]
	s_nop 0
	v_pk_mul_f32 v[20:21], v[12:13], v[18:19] op_sel:[0,1]
	s_nop 0
	v_pk_fma_f32 v[28:29], v[10:11], v[18:19], v[20:21] neg_lo:[0,0,1] neg_hi:[0,0,1]
	v_pk_fma_f32 v[18:19], v[10:11], v[18:19], v[20:21] op_sel_hi:[1,0,1]
	s_nop 0
	v_mov_b32_e32 v29, v19
	v_pk_add_f32 v[18:19], v[28:29], v[154:155]
	s_nop 0
	v_pk_mul_f32 v[20:21], v[12:13], v[18:19] op_sel:[0,1]
	s_nop 0
	v_pk_fma_f32 v[28:29], v[10:11], v[18:19], v[20:21] neg_lo:[0,0,1] neg_hi:[0,0,1]
	v_pk_fma_f32 v[18:19], v[10:11], v[18:19], v[20:21] op_sel_hi:[1,0,1]
	s_nop 0
	v_mov_b32_e32 v29, v19
	v_pk_add_f32 v[18:19], v[28:29], v[156:157]
	s_nop 0
	v_pk_mul_f32 v[20:21], v[12:13], v[18:19] op_sel:[0,1]
	s_nop 0
	v_pk_fma_f32 v[28:29], v[10:11], v[18:19], v[20:21] neg_lo:[0,0,1] neg_hi:[0,0,1]
	v_pk_fma_f32 v[18:19], v[10:11], v[18:19], v[20:21] op_sel_hi:[1,0,1]
	s_nop 0
	v_mov_b32_e32 v29, v19
	v_pk_add_f32 v[18:19], v[28:29], v[158:159]
	s_nop 0
	v_pk_mul_f32 v[20:21], v[12:13], v[18:19] op_sel:[0,1]
	s_nop 0
	v_pk_fma_f32 v[28:29], v[10:11], v[18:19], v[20:21] neg_lo:[0,0,1] neg_hi:[0,0,1]
	v_pk_fma_f32 v[18:19], v[10:11], v[18:19], v[20:21] op_sel_hi:[1,0,1]
	s_nop 0
	v_mov_b32_e32 v29, v19
	v_pk_add_f32 v[18:19], v[28:29], v[160:161]
	s_nop 0
	v_pk_mul_f32 v[20:21], v[12:13], v[18:19] op_sel:[0,1]
	s_nop 0
	v_pk_fma_f32 v[28:29], v[10:11], v[18:19], v[20:21] neg_lo:[0,0,1] neg_hi:[0,0,1]
	v_pk_fma_f32 v[18:19], v[10:11], v[18:19], v[20:21] op_sel_hi:[1,0,1]
	s_nop 0
	v_mov_b32_e32 v29, v19
	v_pk_add_f32 v[18:19], v[28:29], v[162:163]
	s_nop 0
	v_pk_mul_f32 v[20:21], v[12:13], v[18:19] op_sel:[0,1]
	v_pk_fma_f32 v[44:45], v[10:11], v[18:19], v[20:21] neg_lo:[0,0,1] neg_hi:[0,0,1]
	v_pk_fma_f32 v[18:19], v[10:11], v[18:19], v[20:21] op_sel_hi:[1,0,1]
	v_mov_b32_e32 v45, v19
	s_waitcnt vmcnt(16) lgkmcnt(0)
	v_pk_add_f32 v[18:19], v[44:45], v[164:165]
	s_nop 0
	v_pk_mul_f32 v[20:21], v[12:13], v[18:19] op_sel:[0,1]
	s_nop 0
	v_pk_fma_f32 v[28:29], v[10:11], v[18:19], v[20:21] neg_lo:[0,0,1] neg_hi:[0,0,1]
	v_pk_fma_f32 v[18:19], v[10:11], v[18:19], v[20:21] op_sel_hi:[1,0,1]
	s_nop 0
	v_mov_b32_e32 v29, v19
	v_pk_add_f32 v[18:19], v[28:29], v[166:167]
	s_nop 0
	v_pk_mul_f32 v[20:21], v[12:13], v[18:19] op_sel:[0,1]
	s_nop 0
	v_pk_fma_f32 v[28:29], v[10:11], v[18:19], v[20:21] neg_lo:[0,0,1] neg_hi:[0,0,1]
	v_pk_fma_f32 v[18:19], v[10:11], v[18:19], v[20:21] op_sel_hi:[1,0,1]
	s_nop 0
	v_mov_b32_e32 v29, v19
	v_pk_add_f32 v[18:19], v[28:29], v[168:169]
	s_nop 0
	v_pk_mul_f32 v[20:21], v[12:13], v[18:19] op_sel:[0,1]
	s_nop 0
	v_pk_fma_f32 v[28:29], v[10:11], v[18:19], v[20:21] neg_lo:[0,0,1] neg_hi:[0,0,1]
	v_pk_fma_f32 v[18:19], v[10:11], v[18:19], v[20:21] op_sel_hi:[1,0,1]
	s_nop 0
	v_mov_b32_e32 v29, v19
	v_pk_add_f32 v[18:19], v[28:29], v[170:171]
	s_nop 0
	v_pk_mul_f32 v[20:21], v[12:13], v[18:19] op_sel:[0,1]
	s_nop 0
	v_pk_fma_f32 v[28:29], v[10:11], v[18:19], v[20:21] neg_lo:[0,0,1] neg_hi:[0,0,1]
	v_pk_fma_f32 v[18:19], v[10:11], v[18:19], v[20:21] op_sel_hi:[1,0,1]
	s_nop 0
	v_mov_b32_e32 v29, v19
	v_pk_add_f32 v[18:19], v[28:29], v[172:173]
	s_nop 0
	v_pk_mul_f32 v[20:21], v[12:13], v[18:19] op_sel:[0,1]
	s_nop 0
	v_pk_fma_f32 v[28:29], v[10:11], v[18:19], v[20:21] neg_lo:[0,0,1] neg_hi:[0,0,1]
	v_pk_fma_f32 v[18:19], v[10:11], v[18:19], v[20:21] op_sel_hi:[1,0,1]
	s_nop 0
	v_mov_b32_e32 v29, v19
	v_pk_add_f32 v[18:19], v[28:29], v[174:175]
	s_nop 0
	v_pk_mul_f32 v[20:21], v[12:13], v[18:19] op_sel:[0,1]
	s_nop 0
	v_pk_fma_f32 v[28:29], v[10:11], v[18:19], v[20:21] neg_lo:[0,0,1] neg_hi:[0,0,1]
	v_pk_fma_f32 v[18:19], v[10:11], v[18:19], v[20:21] op_sel_hi:[1,0,1]
	s_nop 0
	v_mov_b32_e32 v29, v19
	v_pk_add_f32 v[18:19], v[28:29], v[176:177]
	s_nop 0
	v_pk_mul_f32 v[20:21], v[12:13], v[18:19] op_sel:[0,1]
	s_nop 0
	v_pk_fma_f32 v[28:29], v[10:11], v[18:19], v[20:21] neg_lo:[0,0,1] neg_hi:[0,0,1]
	v_pk_fma_f32 v[18:19], v[10:11], v[18:19], v[20:21] op_sel_hi:[1,0,1]
	s_nop 0
	v_mov_b32_e32 v29, v19
	v_pk_add_f32 v[18:19], v[28:29], v[178:179]
	s_nop 0
	v_pk_mul_f32 v[20:21], v[12:13], v[18:19] op_sel:[0,1]
	v_pk_fma_f32 v[44:45], v[10:11], v[18:19], v[20:21] neg_lo:[0,0,1] neg_hi:[0,0,1]
	v_pk_fma_f32 v[18:19], v[10:11], v[18:19], v[20:21] op_sel_hi:[1,0,1]
	v_mov_b32_e32 v45, v19
	s_waitcnt vmcnt(0) lgkmcnt(0)
	v_pk_add_f32 v[18:19], v[44:45], v[200:201]
	s_nop 0
	v_pk_mul_f32 v[20:21], v[12:13], v[18:19] op_sel:[0,1]
	s_nop 0
	v_pk_fma_f32 v[28:29], v[10:11], v[18:19], v[20:21] neg_lo:[0,0,1] neg_hi:[0,0,1]
	v_pk_fma_f32 v[18:19], v[10:11], v[18:19], v[20:21] op_sel_hi:[1,0,1]
	s_nop 0
	v_mov_b32_e32 v29, v19
	v_pk_add_f32 v[18:19], v[28:29], v[202:203]
	s_nop 0
	v_pk_mul_f32 v[20:21], v[12:13], v[18:19] op_sel:[0,1]
	s_nop 0
	v_pk_fma_f32 v[28:29], v[10:11], v[18:19], v[20:21] neg_lo:[0,0,1] neg_hi:[0,0,1]
	v_pk_fma_f32 v[18:19], v[10:11], v[18:19], v[20:21] op_sel_hi:[1,0,1]
	s_nop 0
	v_mov_b32_e32 v29, v19
	v_pk_add_f32 v[18:19], v[28:29], v[204:205]
	s_nop 0
	v_pk_mul_f32 v[20:21], v[12:13], v[18:19] op_sel:[0,1]
	s_nop 0
	v_pk_fma_f32 v[28:29], v[10:11], v[18:19], v[20:21] neg_lo:[0,0,1] neg_hi:[0,0,1]
	v_pk_fma_f32 v[18:19], v[10:11], v[18:19], v[20:21] op_sel_hi:[1,0,1]
	s_nop 0
	v_mov_b32_e32 v29, v19
	v_pk_add_f32 v[18:19], v[28:29], v[206:207]
	s_nop 0
	v_pk_mul_f32 v[20:21], v[12:13], v[18:19] op_sel:[0,1]
	s_nop 0
	v_pk_fma_f32 v[28:29], v[10:11], v[18:19], v[20:21] neg_lo:[0,0,1] neg_hi:[0,0,1]
	v_pk_fma_f32 v[18:19], v[10:11], v[18:19], v[20:21] op_sel_hi:[1,0,1]
	s_nop 0
	v_mov_b32_e32 v29, v19
	v_pk_add_f32 v[18:19], v[28:29], v[208:209]
	s_nop 0
	v_pk_mul_f32 v[20:21], v[12:13], v[18:19] op_sel:[0,1]
	s_nop 0
	v_pk_fma_f32 v[28:29], v[10:11], v[18:19], v[20:21] neg_lo:[0,0,1] neg_hi:[0,0,1]
	v_pk_fma_f32 v[18:19], v[10:11], v[18:19], v[20:21] op_sel_hi:[1,0,1]
	s_nop 0
	v_mov_b32_e32 v29, v19
	v_pk_add_f32 v[18:19], v[28:29], v[210:211]
	s_nop 0
	v_pk_mul_f32 v[20:21], v[12:13], v[18:19] op_sel:[0,1]
	s_nop 0
	v_pk_fma_f32 v[28:29], v[10:11], v[18:19], v[20:21] neg_lo:[0,0,1] neg_hi:[0,0,1]
	v_pk_fma_f32 v[18:19], v[10:11], v[18:19], v[20:21] op_sel_hi:[1,0,1]
	s_nop 0
	v_mov_b32_e32 v29, v19
	v_pk_add_f32 v[18:19], v[28:29], v[212:213]
	s_nop 0
	v_pk_mul_f32 v[20:21], v[12:13], v[18:19] op_sel:[0,1]
	s_nop 0
	v_pk_fma_f32 v[28:29], v[10:11], v[18:19], v[20:21] neg_lo:[0,0,1] neg_hi:[0,0,1]
	v_pk_fma_f32 v[18:19], v[10:11], v[18:19], v[20:21] op_sel_hi:[1,0,1]
	s_nop 0
	v_mov_b32_e32 v29, v19
	v_pk_add_f32 v[18:19], v[28:29], v[214:215]
	s_mov_b64 s[18:19], 0x4000
	v_mov_b32_e32 v17, 0
	v_mov_b32_e32 v16, v17
	ds_write2st64_b32 v22, v18, v19 offset1:8
	s_waitcnt lgkmcnt(0)
	s_barrier
	s_and_saveexec_b64 s[18:19], s[8:9]
	s_cbranch_execz .LBB0_521
	v_pk_mul_f32 v[16:17], v[10:11], v[10:11]
	s_nop 0
	v_sub_f32_e32 v15, v16, v17
	v_add_f32_e32 v16, v10, v10
	v_mul_f32_e32 v16, v11, v16
	v_mul_f32_e32 v17, v15, v15
	v_add_f32_e32 v15, v15, v15
	v_mul_f32_e32 v15, v16, v15
	v_fma_f32 v17, -v16, v16, v17
	v_mul_f32_e32 v16, v15, v15
	v_fma_f32 v16, v17, v17, -v16
	v_add_f32_e32 v17, v17, v17
	v_mul_f32_e32 v15, v15, v17
	v_mul_f32_e32 v17, v15, v15
	v_fma_f32 v17, v16, v16, -v17
	v_add_f32_e32 v16, v16, v16
	v_mul_f32_e32 v15, v15, v16
	v_mul_f32_e32 v16, v15, v15
	v_fma_f32 v18, v17, v17, -v16
	v_add_f32_e32 v16, v17, v17
	v_mul_f32_e32 v20, v15, v16
	v_mov_b32_e32 v16, v5
	v_mov_b32_e32 v17, v5
	v_mov_b32_e32 v15, 0
	s_and_saveexec_b64 s[20:21], s[10:11]
	s_cbranch_execz .LBB0_516
	v_mov_b32_e32 v16, 0
	v_mov_b32_e32 v19, v18
	v_mov_b32_e32 v21, v20
	s_mov_b32 s15, 0
	s_mov_b64 s[22:23], 0
	v_mov_b32_e32 v15, v25
	v_mov_b32_e32 v17, v16

.LBB0_522:
	v_mov_b32_e32 v54, 0x4f200000
	v_mov_b32_e32 v55, 0
	v_lshl_add_u64 v[52:53], s[2:3], 0, v[18:19]
	v_lshl_add_u64 v[52:53], v[52:53], 0, v[54:55]
	global_load_dword v132, v[52:53], off
	global_load_dword v133, v[52:53], off offset:256
	global_load_dword v134, v[52:53], off offset:512
	global_load_dword v135, v[52:53], off offset:768
	global_load_dword v136, v[52:53], off offset:1024
	global_load_dword v137, v[52:53], off offset:1280
	global_load_dword v138, v[52:53], off offset:1536
	global_load_dword v139, v[52:53], off offset:1792
	global_load_dword v140, v[52:53], off offset:2048
	global_load_dword v141, v[52:53], off offset:2304
	global_load_dword v142, v[52:53], off offset:2560
	global_load_dword v143, v[52:53], off offset:2816
	global_load_dword v144, v[52:53], off offset:3072
	global_load_dword v145, v[52:53], off offset:3328
	global_load_dword v146, v[52:53], off offset:3584
	global_load_dword v147, v[52:53], off offset:3840
	v_lshl_add_u64 v[52:53], v[52:53], 0, s[4:5]
	global_load_dword v148, v[52:53], off
	global_load_dword v149, v[52:53], off offset:256
	global_load_dword v150, v[52:53], off offset:512
	global_load_dword v151, v[52:53], off offset:768
	global_load_dword v152, v[52:53], off offset:1024
	global_load_dword v153, v[52:53], off offset:1280
	global_load_dword v154, v[52:53], off offset:1536
	global_load_dword v155, v[52:53], off offset:1792
	global_load_dword v156, v[52:53], off offset:2048
	global_load_dword v157, v[52:53], off offset:2304
	global_load_dword v158, v[52:53], off offset:2560
	global_load_dword v159, v[52:53], off offset:2816
	global_load_dword v160, v[52:53], off offset:3072
	global_load_dword v161, v[52:53], off offset:3328
	global_load_dword v162, v[52:53], off offset:3584
	global_load_dword v163, v[52:53], off offset:3840
	v_lshl_add_u64 v[52:53], v[52:53], 0, s[4:5]
	global_load_dword v164, v[52:53], off
	global_load_dword v165, v[52:53], off offset:256
	global_load_dword v166, v[52:53], off offset:512
	global_load_dword v167, v[52:53], off offset:768
	global_load_dword v168, v[52:53], off offset:1024
	global_load_dword v169, v[52:53], off offset:1280
	global_load_dword v170, v[52:53], off offset:1536
	global_load_dword v171, v[52:53], off offset:1792
	global_load_dword v172, v[52:53], off offset:2048
	global_load_dword v173, v[52:53], off offset:2304
	global_load_dword v174, v[52:53], off offset:2560
	global_load_dword v175, v[52:53], off offset:2816
	global_load_dword v176, v[52:53], off offset:3072
	global_load_dword v177, v[52:53], off offset:3328
	global_load_dword v178, v[52:53], off offset:3584
	global_load_dword v179, v[52:53], off offset:3840
	v_lshl_add_u64 v[52:53], v[52:53], 0, s[4:5]
	global_load_dword v200, v[52:53], off
	global_load_dword v201, v[52:53], off offset:256
	global_load_dword v202, v[52:53], off offset:512
	global_load_dword v203, v[52:53], off offset:768
	global_load_dword v204, v[52:53], off offset:1024
	global_load_dword v205, v[52:53], off offset:1280
	global_load_dword v206, v[52:53], off offset:1536
	global_load_dword v207, v[52:53], off offset:1792
	global_load_dword v208, v[52:53], off offset:2048
	global_load_dword v209, v[52:53], off offset:2304
	global_load_dword v210, v[52:53], off offset:2560
	global_load_dword v211, v[52:53], off offset:2816
	global_load_dword v212, v[52:53], off offset:3072
	global_load_dword v213, v[52:53], off offset:3328
	global_load_dword v214, v[52:53], off offset:3584
	global_load_dword v215, v[52:53], off offset:3840
	v_bfe_u32 v4, v16, 16, 1
	v_lshl_add_u64 v[20:21], s[2:3], 0, v[14:15]
	v_bfe_u32 v27, v17, 16, 1
	v_pk_mul_f32 v[30:31], v[12:13], v[16:17] op_sel:[0,1]
	v_add3_u32 v4, v16, v4, s30
	v_add3_u32 v27, v17, v27, s30
	v_pk_fma_f32 v[34:35], v[10:11], v[16:17], v[30:31] neg_lo:[0,0,1] neg_hi:[0,0,1]
	v_pk_fma_f32 v[16:17], v[10:11], v[16:17], v[30:31] op_sel_hi:[1,0,1]
	v_add_co_u32_e64 v30, s[14:15], s31, v20
	v_lshl_add_u64 v[28:29], s[2:3], 0, v[18:19]
	s_nop 0
	v_addc_co_u32_e64 v31, s[14:15], 0, v21, s[14:15]
	v_add_co_u32_e64 v36, s[14:15], s33, v20
	v_add_co_u32_e32 v32, vcc, 0x3ca00000, v20
	s_nop 0
	v_addc_co_u32_e64 v37, s[14:15], 0, v21, s[14:15]
	s_mov_b64 s[14:15], vcc
	v_add_co_u32_e32 v28, vcc, s29, v28
	v_mov_b32_e32 v35, v17
	s_nop 0
	v_addc_co_u32_e32 v29, vcc, 0, v29, vcc
	v_addc_co_u32_e64 v33, vcc, 0, v21, s[14:15]
	global_store_short_d16_hi v[32:33], v4, off offset:1024
	global_store_short_d16_hi v[32:33], v27, off offset:1152
	s_add_i32 s16, s16, -8
	v_lshl_add_u64 v[14:15], v[14:15], 0, s[6:7]
	v_lshl_add_u64 v[18:19], v[18:19], 0, s[4:5]
	s_cmp_lg_u32 s16, 0
	s_waitcnt vmcnt(50) lgkmcnt(0)
	v_pk_add_f32 v[20:21], v[34:35], v[132:133]
	s_nop 0
	v_bfe_u32 v4, v20, 16, 1
	v_bfe_u32 v27, v21, 16, 1
	v_pk_mul_f32 v[28:29], v[12:13], v[20:21] op_sel:[0,1]
	v_add3_u32 v4, v20, v4, s30
	v_add3_u32 v27, v21, v27, s30
	v_pk_fma_f32 v[34:35], v[10:11], v[20:21], v[28:29] neg_lo:[0,0,1] neg_hi:[0,0,1]
	v_pk_fma_f32 v[20:21], v[10:11], v[20:21], v[28:29] op_sel_hi:[1,0,1]
	global_store_short_d16_hi v[32:33], v4, off offset:2304
	global_store_short_d16_hi v[32:33], v27, off offset:2432
	v_mov_b32_e32 v35, v21
	v_pk_add_f32 v[20:21], v[34:35], v[134:135]
	s_nop 0
	v_bfe_u32 v4, v20, 16, 1
	v_bfe_u32 v27, v21, 16, 1
	v_pk_mul_f32 v[28:29], v[12:13], v[20:21] op_sel:[0,1]
	v_add3_u32 v4, v20, v4, s30
	v_add3_u32 v27, v21, v27, s30
	v_pk_fma_f32 v[34:35], v[10:11], v[20:21], v[28:29] neg_lo:[0,0,1] neg_hi:[0,0,1]
	v_pk_fma_f32 v[20:21], v[10:11], v[20:21], v[28:29] op_sel_hi:[1,0,1]
	global_store_short_d16_hi v[32:33], v4, off offset:3584
	global_store_short_d16_hi v[32:33], v27, off offset:3712
	v_mov_b32_e32 v35, v21
	v_pk_add_f32 v[20:21], v[34:35], v[136:137]
	s_nop 0
	v_bfe_u32 v4, v20, 16, 1
	v_bfe_u32 v27, v21, 16, 1
	v_pk_mul_f32 v[28:29], v[12:13], v[20:21] op_sel:[0,1]
	v_add3_u32 v4, v20, v4, s30
	v_add3_u32 v27, v21, v27, s30
	v_pk_fma_f32 v[32:33], v[10:11], v[20:21], v[28:29] neg_lo:[0,0,1] neg_hi:[0,0,1]
	v_pk_fma_f32 v[20:21], v[10:11], v[20:21], v[28:29] op_sel_hi:[1,0,1]
	global_store_short_d16_hi v[30:31], v4, off offset:768
	global_store_short_d16_hi v[30:31], v27, off offset:896
	v_mov_b32_e32 v33, v21
	v_pk_add_f32 v[20:21], v[32:33], v[138:139]
	s_nop 0
	v_bfe_u32 v4, v20, 16, 1
	v_bfe_u32 v27, v21, 16, 1
	v_pk_mul_f32 v[28:29], v[12:13], v[20:21] op_sel:[0,1]
	v_add3_u32 v4, v20, v4, s30
	v_add3_u32 v27, v21, v27, s30
	v_pk_fma_f32 v[32:33], v[10:11], v[20:21], v[28:29] neg_lo:[0,0,1] neg_hi:[0,0,1]
	v_pk_fma_f32 v[20:21], v[10:11], v[20:21], v[28:29] op_sel_hi:[1,0,1]
	global_store_short_d16_hi v[30:31], v4, off offset:2048
	global_store_short_d16_hi v[30:31], v27, off offset:2176
	v_mov_b32_e32 v33, v21
	v_pk_add_f32 v[20:21], v[32:33], v[140:141]
	s_nop 0
	v_bfe_u32 v4, v20, 16, 1
	v_bfe_u32 v27, v21, 16, 1
	v_pk_mul_f32 v[28:29], v[12:13], v[20:21] op_sel:[0,1]
	v_add3_u32 v4, v20, v4, s30
	v_add3_u32 v27, v21, v27, s30
	v_pk_fma_f32 v[32:33], v[10:11], v[20:21], v[28:29] neg_lo:[0,0,1] neg_hi:[0,0,1]
	v_pk_fma_f32 v[20:21], v[10:11], v[20:21], v[28:29] op_sel_hi:[1,0,1]
	global_store_short_d16_hi v[30:31], v4, off offset:3328
	global_store_short_d16_hi v[30:31], v27, off offset:3456
	v_mov_b32_e32 v33, v21
	v_pk_add_f32 v[20:21], v[32:33], v[142:143]
	s_nop 0
	v_bfe_u32 v4, v20, 16, 1
	v_bfe_u32 v27, v21, 16, 1
	v_pk_mul_f32 v[28:29], v[12:13], v[20:21] op_sel:[0,1]
	v_add3_u32 v4, v20, v4, s30
	v_add3_u32 v27, v21, v27, s30
	v_pk_fma_f32 v[30:31], v[10:11], v[20:21], v[28:29] neg_lo:[0,0,1] neg_hi:[0,0,1]
	v_pk_fma_f32 v[20:21], v[10:11], v[20:21], v[28:29] op_sel_hi:[1,0,1]
	global_store_short_d16_hi v[36:37], v4, off offset:512
	global_store_short_d16_hi v[36:37], v27, off offset:640
	v_mov_b32_e32 v31, v21
	v_pk_add_f32 v[20:21], v[30:31], v[144:145]
	s_nop 0
	v_bfe_u32 v4, v20, 16, 1
	v_bfe_u32 v27, v21, 16, 1
	v_pk_mul_f32 v[28:29], v[12:13], v[20:21] op_sel:[0,1]
	v_add3_u32 v4, v20, v4, s30
	v_add3_u32 v27, v21, v27, s30
	v_pk_fma_f32 v[30:31], v[10:11], v[20:21], v[28:29] neg_lo:[0,0,1] neg_hi:[0,0,1]
	v_pk_fma_f32 v[20:21], v[10:11], v[20:21], v[28:29] op_sel_hi:[1,0,1]
	global_store_short_d16_hi v[36:37], v4, off offset:1792
	global_store_short_d16_hi v[36:37], v27, off offset:1920
	v_mov_b32_e32 v31, v21
	v_pk_add_f32 v[16:17], v[30:31], v[146:147]
	s_nop 0
	v_bfe_u32 v4, v16, 16, 1
	v_lshl_add_u64 v[20:21], s[2:3], 0, v[14:15]
	v_bfe_u32 v27, v17, 16, 1
	v_pk_mul_f32 v[30:31], v[12:13], v[16:17] op_sel:[0,1]
	v_add3_u32 v4, v16, v4, s30
	v_add3_u32 v27, v17, v27, s30
	v_pk_fma_f32 v[34:35], v[10:11], v[16:17], v[30:31] neg_lo:[0,0,1] neg_hi:[0,0,1]
	v_pk_fma_f32 v[16:17], v[10:11], v[16:17], v[30:31] op_sel_hi:[1,0,1]
	v_add_co_u32_e64 v30, s[14:15], s31, v20
	v_lshl_add_u64 v[28:29], s[2:3], 0, v[18:19]
	s_nop 0
	v_addc_co_u32_e64 v31, s[14:15], 0, v21, s[14:15]
	v_add_co_u32_e64 v36, s[14:15], s33, v20
	v_add_co_u32_e32 v32, vcc, 0x3ca00000, v20
	s_nop 0
	v_addc_co_u32_e64 v37, s[14:15], 0, v21, s[14:15]
	s_mov_b64 s[14:15], vcc
	v_add_co_u32_e32 v28, vcc, s29, v28
	v_mov_b32_e32 v35, v17
	s_nop 0
	v_addc_co_u32_e32 v29, vcc, 0, v29, vcc
	v_addc_co_u32_e64 v33, vcc, 0, v21, s[14:15]
	global_store_short_d16_hi v[32:33], v4, off offset:1024
	global_store_short_d16_hi v[32:33], v27, off offset:1152
	s_add_i32 s16, s16, -8
	v_lshl_add_u64 v[14:15], v[14:15], 0, s[6:7]
	v_lshl_add_u64 v[18:19], v[18:19], 0, s[4:5]
	s_cmp_lg_u32 s16, 0
	s_waitcnt vmcnt(50) lgkmcnt(0)
	v_pk_add_f32 v[20:21], v[34:35], v[148:149]
	s_nop 0
	v_bfe_u32 v4, v20, 16, 1
	v_bfe_u32 v27, v21, 16, 1
	v_pk_mul_f32 v[28:29], v[12:13], v[20:21] op_sel:[0,1]
	v_add3_u32 v4, v20, v4, s30
	v_add3_u32 v27, v21, v27, s30
	v_pk_fma_f32 v[34:35], v[10:11], v[20:21], v[28:29] neg_lo:[0,0,1] neg_hi:[0,0,1]
	v_pk_fma_f32 v[20:21], v[10:11], v[20:21], v[28:29] op_sel_hi:[1,0,1]
	global_store_short_d16_hi v[32:33], v4, off offset:2304
	global_store_short_d16_hi v[32:33], v27, off offset:2432
	v_mov_b32_e32 v35, v21
	v_pk_add_f32 v[20:21], v[34:35], v[150:151]
	s_nop 0
	v_bfe_u32 v4, v20, 16, 1
	v_bfe_u32 v27, v21, 16, 1
	v_pk_mul_f32 v[28:29], v[12:13], v[20:21] op_sel:[0,1]
	v_add3_u32 v4, v20, v4, s30
	v_add3_u32 v27, v21, v27, s30
	v_pk_fma_f32 v[34:35], v[10:11], v[20:21], v[28:29] neg_lo:[0,0,1] neg_hi:[0,0,1]
	v_pk_fma_f32 v[20:21], v[10:11], v[20:21], v[28:29] op_sel_hi:[1,0,1]
	global_store_short_d16_hi v[32:33], v4, off offset:3584
	global_store_short_d16_hi v[32:33], v27, off offset:3712
	v_mov_b32_e32 v35, v21
	v_pk_add_f32 v[20:21], v[34:35], v[152:153]
	s_nop 0
	v_bfe_u32 v4, v20, 16, 1
	v_bfe_u32 v27, v21, 16, 1
	v_pk_mul_f32 v[28:29], v[12:13], v[20:21] op_sel:[0,1]
	v_add3_u32 v4, v20, v4, s30
	v_add3_u32 v27, v21, v27, s30
	v_pk_fma_f32 v[32:33], v[10:11], v[20:21], v[28:29] neg_lo:[0,0,1] neg_hi:[0,0,1]
	v_pk_fma_f32 v[20:21], v[10:11], v[20:21], v[28:29] op_sel_hi:[1,0,1]
	global_store_short_d16_hi v[30:31], v4, off offset:768
	global_store_short_d16_hi v[30:31], v27, off offset:896
	v_mov_b32_e32 v33, v21
	v_pk_add_f32 v[20:21], v[32:33], v[154:155]
	s_nop 0
	v_bfe_u32 v4, v20, 16, 1
	v_bfe_u32 v27, v21, 16, 1
	v_pk_mul_f32 v[28:29], v[12:13], v[20:21] op_sel:[0,1]
	v_add3_u32 v4, v20, v4, s30
	v_add3_u32 v27, v21, v27, s30
	v_pk_fma_f32 v[32:33], v[10:11], v[20:21], v[28:29] neg_lo:[0,0,1] neg_hi:[0,0,1]
	v_pk_fma_f32 v[20:21], v[10:11], v[20:21], v[28:29] op_sel_hi:[1,0,1]
	global_store_short_d16_hi v[30:31], v4, off offset:2048
	global_store_short_d16_hi v[30:31], v27, off offset:2176
	v_mov_b32_e32 v33, v21
	v_pk_add_f32 v[20:21], v[32:33], v[156:157]
	s_nop 0
	v_bfe_u32 v4, v20, 16, 1
	v_bfe_u32 v27, v21, 16, 1
	v_pk_mul_f32 v[28:29], v[12:13], v[20:21] op_sel:[0,1]
	v_add3_u32 v4, v20, v4, s30
	v_add3_u32 v27, v21, v27, s30
	v_pk_fma_f32 v[32:33], v[10:11], v[20:21], v[28:29] neg_lo:[0,0,1] neg_hi:[0,0,1]
	v_pk_fma_f32 v[20:21], v[10:11], v[20:21], v[28:29] op_sel_hi:[1,0,1]
	global_store_short_d16_hi v[30:31], v4, off offset:3328
	global_store_short_d16_hi v[30:31], v27, off offset:3456
	v_mov_b32_e32 v33, v21
	v_pk_add_f32 v[20:21], v[32:33], v[158:159]
	s_nop 0
	v_bfe_u32 v4, v20, 16, 1
	v_bfe_u32 v27, v21, 16, 1
	v_pk_mul_f32 v[28:29], v[12:13], v[20:21] op_sel:[0,1]
	v_add3_u32 v4, v20, v4, s30
	v_add3_u32 v27, v21, v27, s30
	v_pk_fma_f32 v[30:31], v[10:11], v[20:21], v[28:29] neg_lo:[0,0,1] neg_hi:[0,0,1]
	v_pk_fma_f32 v[20:21], v[10:11], v[20:21], v[28:29] op_sel_hi:[1,0,1]
	global_store_short_d16_hi v[36:37], v4, off offset:512
	global_store_short_d16_hi v[36:37], v27, off offset:640
	v_mov_b32_e32 v31, v21
	v_pk_add_f32 v[20:21], v[30:31], v[160:161]
	s_nop 0
	v_bfe_u32 v4, v20, 16, 1
	v_bfe_u32 v27, v21, 16, 1
	v_pk_mul_f32 v[28:29], v[12:13], v[20:21] op_sel:[0,1]
	v_add3_u32 v4, v20, v4, s30
	v_add3_u32 v27, v21, v27, s30
	v_pk_fma_f32 v[30:31], v[10:11], v[20:21], v[28:29] neg_lo:[0,0,1] neg_hi:[0,0,1]
	v_pk_fma_f32 v[20:21], v[10:11], v[20:21], v[28:29] op_sel_hi:[1,0,1]
	global_store_short_d16_hi v[36:37], v4, off offset:1792
	global_store_short_d16_hi v[36:37], v27, off offset:1920
	v_mov_b32_e32 v31, v21
	v_pk_add_f32 v[16:17], v[30:31], v[162:163]
	s_nop 0
	v_bfe_u32 v4, v16, 16, 1
	v_lshl_add_u64 v[20:21], s[2:3], 0, v[14:15]
	v_bfe_u32 v27, v17, 16, 1
	v_pk_mul_f32 v[30:31], v[12:13], v[16:17] op_sel:[0,1]
	v_add3_u32 v4, v16, v4, s30
	v_add3_u32 v27, v17, v27, s30
	v_pk_fma_f32 v[34:35], v[10:11], v[16:17], v[30:31] neg_lo:[0,0,1] neg_hi:[0,0,1]
	v_pk_fma_f32 v[16:17], v[10:11], v[16:17], v[30:31] op_sel_hi:[1,0,1]
	v_add_co_u32_e64 v30, s[14:15], s31, v20
	v_lshl_add_u64 v[28:29], s[2:3], 0, v[18:19]
	s_nop 0
	v_addc_co_u32_e64 v31, s[14:15], 0, v21, s[14:15]
	v_add_co_u32_e64 v36, s[14:15], s33, v20
	v_add_co_u32_e32 v32, vcc, 0x3ca00000, v20
	s_nop 0
	v_addc_co_u32_e64 v37, s[14:15], 0, v21, s[14:15]
	s_mov_b64 s[14:15], vcc
	v_add_co_u32_e32 v28, vcc, s29, v28
	v_mov_b32_e32 v35, v17
	s_nop 0
	v_addc_co_u32_e32 v29, vcc, 0, v29, vcc
	v_addc_co_u32_e64 v33, vcc, 0, v21, s[14:15]
	global_store_short_d16_hi v[32:33], v4, off offset:1024
	global_store_short_d16_hi v[32:33], v27, off offset:1152
	s_add_i32 s16, s16, -8
	v_lshl_add_u64 v[14:15], v[14:15], 0, s[6:7]
	v_lshl_add_u64 v[18:19], v[18:19], 0, s[4:5]
	s_cmp_lg_u32 s16, 0
	s_waitcnt vmcnt(50) lgkmcnt(0)
	v_pk_add_f32 v[20:21], v[34:35], v[164:165]
	s_nop 0
	v_bfe_u32 v4, v20, 16, 1
	v_bfe_u32 v27, v21, 16, 1
	v_pk_mul_f32 v[28:29], v[12:13], v[20:21] op_sel:[0,1]
	v_add3_u32 v4, v20, v4, s30
	v_add3_u32 v27, v21, v27, s30
	v_pk_fma_f32 v[34:35], v[10:11], v[20:21], v[28:29] neg_lo:[0,0,1] neg_hi:[0,0,1]
	v_pk_fma_f32 v[20:21], v[10:11], v[20:21], v[28:29] op_sel_hi:[1,0,1]
	global_store_short_d16_hi v[32:33], v4, off offset:2304
	global_store_short_d16_hi v[32:33], v27, off offset:2432
	v_mov_b32_e32 v35, v21
	v_pk_add_f32 v[20:21], v[34:35], v[166:167]
	s_nop 0
	v_bfe_u32 v4, v20, 16, 1
	v_bfe_u32 v27, v21, 16, 1
	v_pk_mul_f32 v[28:29], v[12:13], v[20:21] op_sel:[0,1]
	v_add3_u32 v4, v20, v4, s30
	v_add3_u32 v27, v21, v27, s30
	v_pk_fma_f32 v[34:35], v[10:11], v[20:21], v[28:29] neg_lo:[0,0,1] neg_hi:[0,0,1]
	v_pk_fma_f32 v[20:21], v[10:11], v[20:21], v[28:29] op_sel_hi:[1,0,1]
	global_store_short_d16_hi v[32:33], v4, off offset:3584
	global_store_short_d16_hi v[32:33], v27, off offset:3712
	v_mov_b32_e32 v35, v21
	v_pk_add_f32 v[20:21], v[34:35], v[168:169]
	s_nop 0
	v_bfe_u32 v4, v20, 16, 1
	v_bfe_u32 v27, v21, 16, 1
	v_pk_mul_f32 v[28:29], v[12:13], v[20:21] op_sel:[0,1]
	v_add3_u32 v4, v20, v4, s30
	v_add3_u32 v27, v21, v27, s30
	v_pk_fma_f32 v[32:33], v[10:11], v[20:21], v[28:29] neg_lo:[0,0,1] neg_hi:[0,0,1]
	v_pk_fma_f32 v[20:21], v[10:11], v[20:21], v[28:29] op_sel_hi:[1,0,1]
	global_store_short_d16_hi v[30:31], v4, off offset:768
	global_store_short_d16_hi v[30:31], v27, off offset:896
	v_mov_b32_e32 v33, v21
	v_pk_add_f32 v[20:21], v[32:33], v[170:171]
	s_nop 0
	v_bfe_u32 v4, v20, 16, 1
	v_bfe_u32 v27, v21, 16, 1
	v_pk_mul_f32 v[28:29], v[12:13], v[20:21] op_sel:[0,1]
	v_add3_u32 v4, v20, v4, s30
	v_add3_u32 v27, v21, v27, s30
	v_pk_fma_f32 v[32:33], v[10:11], v[20:21], v[28:29] neg_lo:[0,0,1] neg_hi:[0,0,1]
	v_pk_fma_f32 v[20:21], v[10:11], v[20:21], v[28:29] op_sel_hi:[1,0,1]
	global_store_short_d16_hi v[30:31], v4, off offset:2048
	global_store_short_d16_hi v[30:31], v27, off offset:2176
	v_mov_b32_e32 v33, v21
	v_pk_add_f32 v[20:21], v[32:33], v[172:173]
	s_nop 0
	v_bfe_u32 v4, v20, 16, 1
	v_bfe_u32 v27, v21, 16, 1
	v_pk_mul_f32 v[28:29], v[12:13], v[20:21] op_sel:[0,1]
	v_add3_u32 v4, v20, v4, s30
	v_add3_u32 v27, v21, v27, s30
	v_pk_fma_f32 v[32:33], v[10:11], v[20:21], v[28:29] neg_lo:[0,0,1] neg_hi:[0,0,1]
	v_pk_fma_f32 v[20:21], v[10:11], v[20:21], v[28:29] op_sel_hi:[1,0,1]
	global_store_short_d16_hi v[30:31], v4, off offset:3328
	global_store_short_d16_hi v[30:31], v27, off offset:3456
	v_mov_b32_e32 v33, v21
	v_pk_add_f32 v[20:21], v[32:33], v[174:175]
	s_nop 0
	v_bfe_u32 v4, v20, 16, 1
	v_bfe_u32 v27, v21, 16, 1
	v_pk_mul_f32 v[28:29], v[12:13], v[20:21] op_sel:[0,1]
	v_add3_u32 v4, v20, v4, s30
	v_add3_u32 v27, v21, v27, s30
	v_pk_fma_f32 v[30:31], v[10:11], v[20:21], v[28:29] neg_lo:[0,0,1] neg_hi:[0,0,1]
	v_pk_fma_f32 v[20:21], v[10:11], v[20:21], v[28:29] op_sel_hi:[1,0,1]
	global_store_short_d16_hi v[36:37], v4, off offset:512
	global_store_short_d16_hi v[36:37], v27, off offset:640
	v_mov_b32_e32 v31, v21
	v_pk_add_f32 v[20:21], v[30:31], v[176:177]
	s_nop 0
	v_bfe_u32 v4, v20, 16, 1
	v_bfe_u32 v27, v21, 16, 1
	v_pk_mul_f32 v[28:29], v[12:13], v[20:21] op_sel:[0,1]
	v_add3_u32 v4, v20, v4, s30
	v_add3_u32 v27, v21, v27, s30
	v_pk_fma_f32 v[30:31], v[10:11], v[20:21], v[28:29] neg_lo:[0,0,1] neg_hi:[0,0,1]
	v_pk_fma_f32 v[20:21], v[10:11], v[20:21], v[28:29] op_sel_hi:[1,0,1]
	global_store_short_d16_hi v[36:37], v4, off offset:1792
	global_store_short_d16_hi v[36:37], v27, off offset:1920
	v_mov_b32_e32 v31, v21
	v_pk_add_f32 v[16:17], v[30:31], v[178:179]
	s_nop 0
	v_bfe_u32 v4, v16, 16, 1
	v_lshl_add_u64 v[20:21], s[2:3], 0, v[14:15]
	v_bfe_u32 v27, v17, 16, 1
	v_pk_mul_f32 v[30:31], v[12:13], v[16:17] op_sel:[0,1]
	v_add3_u32 v4, v16, v4, s30
	v_add3_u32 v27, v17, v27, s30
	v_pk_fma_f32 v[34:35], v[10:11], v[16:17], v[30:31] neg_lo:[0,0,1] neg_hi:[0,0,1]
	v_pk_fma_f32 v[16:17], v[10:11], v[16:17], v[30:31] op_sel_hi:[1,0,1]
	v_add_co_u32_e64 v30, s[14:15], s31, v20
	v_lshl_add_u64 v[28:29], s[2:3], 0, v[18:19]
	s_nop 0
	v_addc_co_u32_e64 v31, s[14:15], 0, v21, s[14:15]
	v_add_co_u32_e64 v36, s[14:15], s33, v20
	v_add_co_u32_e32 v32, vcc, 0x3ca00000, v20
	s_nop 0
	v_addc_co_u32_e64 v37, s[14:15], 0, v21, s[14:15]
	s_mov_b64 s[14:15], vcc
	v_add_co_u32_e32 v28, vcc, s29, v28
	v_mov_b32_e32 v35, v17
	s_nop 0
	v_addc_co_u32_e32 v29, vcc, 0, v29, vcc
	v_addc_co_u32_e64 v33, vcc, 0, v21, s[14:15]
	global_store_short_d16_hi v[32:33], v4, off offset:1024
	global_store_short_d16_hi v[32:33], v27, off offset:1152
	s_add_i32 s16, s16, -8
	v_lshl_add_u64 v[14:15], v[14:15], 0, s[6:7]
	v_lshl_add_u64 v[18:19], v[18:19], 0, s[4:5]
	s_cmp_lg_u32 s16, 0
	s_waitcnt vmcnt(50) lgkmcnt(0)
	v_pk_add_f32 v[20:21], v[34:35], v[200:201]
	s_nop 0
	v_bfe_u32 v4, v20, 16, 1
	v_bfe_u32 v27, v21, 16, 1
	v_pk_mul_f32 v[28:29], v[12:13], v[20:21] op_sel:[0,1]
	v_add3_u32 v4, v20, v4, s30
	v_add3_u32 v27, v21, v27, s30
	v_pk_fma_f32 v[34:35], v[10:11], v[20:21], v[28:29] neg_lo:[0,0,1] neg_hi:[0,0,1]
	v_pk_fma_f32 v[20:21], v[10:11], v[20:21], v[28:29] op_sel_hi:[1,0,1]
	global_store_short_d16_hi v[32:33], v4, off offset:2304
	global_store_short_d16_hi v[32:33], v27, off offset:2432
	v_mov_b32_e32 v35, v21
	v_pk_add_f32 v[20:21], v[34:35], v[202:203]
	s_nop 0
	v_bfe_u32 v4, v20, 16, 1
	v_bfe_u32 v27, v21, 16, 1
	v_pk_mul_f32 v[28:29], v[12:13], v[20:21] op_sel:[0,1]
	v_add3_u32 v4, v20, v4, s30
	v_add3_u32 v27, v21, v27, s30
	v_pk_fma_f32 v[34:35], v[10:11], v[20:21], v[28:29] neg_lo:[0,0,1] neg_hi:[0,0,1]
	v_pk_fma_f32 v[20:21], v[10:11], v[20:21], v[28:29] op_sel_hi:[1,0,1]
	global_store_short_d16_hi v[32:33], v4, off offset:3584
	global_store_short_d16_hi v[32:33], v27, off offset:3712
	v_mov_b32_e32 v35, v21
	v_pk_add_f32 v[20:21], v[34:35], v[204:205]
	s_nop 0
	v_bfe_u32 v4, v20, 16, 1
	v_bfe_u32 v27, v21, 16, 1
	v_pk_mul_f32 v[28:29], v[12:13], v[20:21] op_sel:[0,1]
	v_add3_u32 v4, v20, v4, s30
	v_add3_u32 v27, v21, v27, s30
	v_pk_fma_f32 v[32:33], v[10:11], v[20:21], v[28:29] neg_lo:[0,0,1] neg_hi:[0,0,1]
	v_pk_fma_f32 v[20:21], v[10:11], v[20:21], v[28:29] op_sel_hi:[1,0,1]
	global_store_short_d16_hi v[30:31], v4, off offset:768
	global_store_short_d16_hi v[30:31], v27, off offset:896
	v_mov_b32_e32 v33, v21
	v_pk_add_f32 v[20:21], v[32:33], v[206:207]
	s_nop 0
	v_bfe_u32 v4, v20, 16, 1
	v_bfe_u32 v27, v21, 16, 1
	v_pk_mul_f32 v[28:29], v[12:13], v[20:21] op_sel:[0,1]
	v_add3_u32 v4, v20, v4, s30
	v_add3_u32 v27, v21, v27, s30
	v_pk_fma_f32 v[32:33], v[10:11], v[20:21], v[28:29] neg_lo:[0,0,1] neg_hi:[0,0,1]
	v_pk_fma_f32 v[20:21], v[10:11], v[20:21], v[28:29] op_sel_hi:[1,0,1]
	global_store_short_d16_hi v[30:31], v4, off offset:2048
	global_store_short_d16_hi v[30:31], v27, off offset:2176
	v_mov_b32_e32 v33, v21
	v_pk_add_f32 v[20:21], v[32:33], v[208:209]
	s_nop 0
	v_bfe_u32 v4, v20, 16, 1
	v_bfe_u32 v27, v21, 16, 1
	v_pk_mul_f32 v[28:29], v[12:13], v[20:21] op_sel:[0,1]
	v_add3_u32 v4, v20, v4, s30
	v_add3_u32 v27, v21, v27, s30
	v_pk_fma_f32 v[32:33], v[10:11], v[20:21], v[28:29] neg_lo:[0,0,1] neg_hi:[0,0,1]
	v_pk_fma_f32 v[20:21], v[10:11], v[20:21], v[28:29] op_sel_hi:[1,0,1]
	global_store_short_d16_hi v[30:31], v4, off offset:3328
	global_store_short_d16_hi v[30:31], v27, off offset:3456
	v_mov_b32_e32 v33, v21
	v_pk_add_f32 v[20:21], v[32:33], v[210:211]
	s_nop 0
	v_bfe_u32 v4, v20, 16, 1
	v_bfe_u32 v27, v21, 16, 1
	v_pk_mul_f32 v[28:29], v[12:13], v[20:21] op_sel:[0,1]
	v_add3_u32 v4, v20, v4, s30
	v_add3_u32 v27, v21, v27, s30
	v_pk_fma_f32 v[30:31], v[10:11], v[20:21], v[28:29] neg_lo:[0,0,1] neg_hi:[0,0,1]
	v_pk_fma_f32 v[20:21], v[10:11], v[20:21], v[28:29] op_sel_hi:[1,0,1]
	global_store_short_d16_hi v[36:37], v4, off offset:512
	global_store_short_d16_hi v[36:37], v27, off offset:640
	v_mov_b32_e32 v31, v21
	v_pk_add_f32 v[20:21], v[30:31], v[212:213]
	s_nop 0
	v_bfe_u32 v4, v20, 16, 1
	v_bfe_u32 v27, v21, 16, 1
	v_pk_mul_f32 v[28:29], v[12:13], v[20:21] op_sel:[0,1]
	v_add3_u32 v4, v20, v4, s30
	v_add3_u32 v27, v21, v27, s30
	v_pk_fma_f32 v[30:31], v[10:11], v[20:21], v[28:29] neg_lo:[0,0,1] neg_hi:[0,0,1]
	v_pk_fma_f32 v[20:21], v[10:11], v[20:21], v[28:29] op_sel_hi:[1,0,1]
	global_store_short_d16_hi v[36:37], v4, off offset:1792
	global_store_short_d16_hi v[36:37], v27, off offset:1920
	v_mov_b32_e32 v31, v21
	v_pk_add_f32 v[16:17], v[30:31], v[214:215]
	s_add_i32 s24, s24, s80
	s_add_i32 s27, s27, s28
	s_cmpk_gt_i32 s24, 0x7f
	s_waitcnt lgkmcnt(0)
	s_barrier
	s_cbranch_scc0 .LBB0_509
